# lever 2 (prologue de-serialisation): NA unit's first K/V tile loads issued ahead of the workgroup barrier instead of behind it
# baseline (speedup 1.0000x reference)
; #define NA_STORE(bufp) do { _Pragma("unroll") for (int i_ = 0; i_ < 4; ++i_) { const int id = tid + 512 * i_, key = id >> 4, ch = id & 15; \
;         *(LAS u32x4*)((bufp) + NA_KB + key * NA_RSK + ch * 16) = rk[i_]; *(LAS u32x4*)((bufp) + NA_VB + key * NA_RSV + ch * 16) = rv[i_]; } } while (0)
; __device__ __forceinline__ void na_fast_unit(int unit, const bf16_t* P, const float* rpb, bf16_t* AO, LAS unsigned char* lds) {
;     ...
;     const int rstart = min(max(r - 4, 0), 56);
;     const int col = 16 * cq + l15, cstart = min(max(col - 8, 0), 48);
;     const int ct0 = min(max(cq - 1, 0), 1);
;     const float scale = 0.08838834764831845f;
;     bf16x8 qf[4];
;     { const bf16_t* qp = P + (size_t)(b * T + r * 64 + col) * LDP1 + h * 128 + 8 * q;
; #pragma unroll
;         for (int kk = 0; kk < 4; ++kk) qf[kk] = *(const bf16x8*)(qp + 32 * kk); }
;     u32x4 rk[4], rv[4];
;     ...
;     float m = -1.0e30f, l = 0.f;
;     f32x4 accO[8];
; #pragma unroll
;     for (int c = 0; c < 8; ++c) accO[c] = (f32x4){0.f, 0.f, 0.f, 0.f};
;     __syncthreads();
;     NA_LOAD(0); NA_STORE(lds);
;     __syncthreads();
.LBB0_1213:
	s_or_b64 exec, exec, s[2:3]
	s_waitcnt lgkmcnt(0)
	s_barrier
	ds_read_b32 v2, v125
	s_movk_i32 s2, 0x7ff
	s_waitcnt lgkmcnt(0)
	v_cmp_lt_u32_e32 vcc, s2, v2
	v_readfirstlane_b32 s6, v2
	s_mov_b64 s[2:3], -1
	s_cbranch_vccnz .LBB0_1208
	s_and_b32 s16, s6, 63
	s_lshr_b32 s53, s6, 9
	v_readfirstlane_b32 s50, v0
	v_sub_u32_e64 v2, s16, 4 clamp
	s_lshl_b32 s54, s53, 12
	s_lshl_b32 s2, s16, 6
	s_bfe_u32 s51, s50, 0x20006
	s_or_b32 s49, s54, s2
	v_readfirstlane_b32 s2, v2
	s_lshl_b32 s48, s51, 4
	s_min_u32 s55, s2, 56
	s_bfe_u32 s56, s6, 0x30006
	v_or_b32_e32 v50, s48, v1
	s_lshl_b32 s6, s55, 6
	s_or_b32 s2, s54, s6
	v_or_b32_e32 v2, s49, v50
	s_movk_i32 s3, 0x1900
	v_readlane_b32 s18, v254, 61
	v_mul_lo_u32 v86, v2, s3
	v_readlane_b32 s19, v254, 62
	v_or_b32_e32 v18, s2, v168
	s_lshl_b32 s24, s56, 8
	v_lshl_add_u64 v[2:3], v[86:87], 1, s[18:19]
	v_mul_lo_u32 v86, v18, s46
	v_lshl_add_u64 v[18:19], s[18:19], 0, v[86:87]
	v_mov_b64_e32 v[42:43], s[18:19]
	v_lshl_add_u64 v[18:19], v[18:19], 0, s[24:25]
	v_mov_b32_e32 v93, v87
	v_or_b32_e32 v26, s2, v170
	v_or_b32_e32 v178, s54, v104
	v_lshl_add_u64 v[18:19], v[18:19], 0, v[92:93]
	v_mad_u64_u32 v[26:27], s[2:3], v26, s46, v[42:43]
	v_add_u32_e32 v34, s6, v178
	v_lshl_add_u64 v[22:23], v[18:19], 0, s[10:11]
	v_add_co_u32_e32 v18, vcc, s47, v18
	v_lshl_add_u64 v[26:27], v[26:27], 0, s[24:25]
	v_mul_lo_u32 v86, v34, s46
	v_add_u32_e64 v44, s55, 1
	v_addc_co_u32_e32 v19, vcc, 0, v19, vcc
	v_lshl_add_u64 v[26:27], v[26:27], 0, v[92:93]
	v_lshl_add_u64 v[34:35], s[18:19], 0, v[86:87]
	v_lshl_add_u32 v44, v44, 6, s54
	v_lshl_add_u64 v[30:31], v[26:27], 0, s[10:11]
	v_add_co_u32_e32 v26, vcc, s47, v26
	v_lshl_add_u64 v[34:35], v[34:35], 0, s[24:25]
	v_or_b32_e32 v44, v44, v106
	v_addc_co_u32_e32 v27, vcc, 0, v27, vcc
	v_lshl_add_u64 v[34:35], v[34:35], 0, v[92:93]
	v_mad_u64_u32 v[42:43], s[2:3], v44, s46, v[42:43]
	v_lshl_add_u64 v[38:39], v[34:35], 0, s[10:11]
	v_add_co_u32_e32 v34, vcc, s47, v34
	v_lshl_add_u64 v[42:43], v[42:43], 0, s[24:25]
	s_nop 0
	v_addc_co_u32_e32 v35, vcc, 0, v35, vcc
	v_lshl_add_u64 v[42:43], v[42:43], 0, v[92:93]
	v_lshl_add_u64 v[2:3], v[2:3], 0, s[24:25]
	v_mov_b32_e32 v91, v87
	v_lshl_add_u64 v[46:47], v[42:43], 0, s[10:11]
	v_add_co_u32_e32 v42, vcc, s47, v42
	v_lshl_add_u64 v[2:3], v[2:3], 0, v[90:91]
	s_nop 0
	v_addc_co_u32_e32 v43, vcc, 0, v43, vcc
	global_load_dwordx4 v[14:17], v[2:3], off
	global_load_dwordx4 v[10:13], v[2:3], off offset:64
	global_load_dwordx4 v[6:9], v[2:3], off offset:128
	s_nop 0
	global_load_dwordx4 v[2:5], v[2:3], off offset:192
	global_load_dwordx4 v[18:21], v[18:19], off offset:1024
	s_nop 0
	global_load_dwordx4 v[22:25], v[22:23], off offset:2048
	s_nop 0
	global_load_dwordx4 v[26:29], v[26:27], off offset:1024
	s_nop 0
	global_load_dwordx4 v[30:33], v[30:31], off offset:2048
	s_nop 0
	global_load_dwordx4 v[34:37], v[34:35], off offset:1024
	s_nop 0
	global_load_dwordx4 v[38:41], v[38:39], off offset:2048
	s_nop 0
	global_load_dwordx4 v[42:45], v[42:43], off offset:1024
	s_nop 0
	global_load_dwordx4 v[46:49], v[46:47], off offset:2048
	s_barrier
	s_lshr_b32 s52, s50, 8
	s_lshl_b32 s57, s52, 6
	s_cmp_gt_u32 s51, 1
	s_cselect_b64 s[2:3], -1, 0
	s_and_b64 s[6:7], s[2:3], exec
	s_cselect_b32 s33, 16, 0
	s_add_i32 s6, s55, 2
	s_lshl_b32 s7, s6, 6
	s_add_i32 s14, s7, s54
	v_or_b32_e32 v182, s54, v170
	v_or_b32_e32 v179, s54, v106
	v_or_b32_e32 v138, s57, v1
	v_sub_u32_e64 v51, v50, 8 clamp
	v_lshlrev_b32_e32 v54, 2, v50
	v_or_b32_e32 v50, s33, v138
	v_mul_lo_u32 v82, v50, s13
	v_add_u32_e32 v180, v120, v82
	v_min_u32_e32 v62, 48, v51
	v_readlane_b32 s60, v254, 29
	v_readlane_b32 s64, v254, 33
	v_readlane_b32 s65, v254, 34
	s_waitcnt vmcnt(7)
	ds_write_b128 v126, v[18:21]
	s_waitcnt vmcnt(6)
	ds_write_b128 v127, v[22:25] offset:34816
	s_waitcnt vmcnt(5)
	ds_write_b128 v128, v[26:29]
	s_waitcnt vmcnt(4)
	ds_write_b128 v129, v[30:33] offset:34816
	s_waitcnt vmcnt(3)
	ds_write_b128 v126, v[34:37] offset:17408
	s_waitcnt vmcnt(2)
	ds_write_b128 v130, v[38:41] offset:34816
	s_waitcnt vmcnt(1)
	ds_write_b128 v131, v[42:45]
	s_waitcnt vmcnt(0)
	ds_write_b128 v132, v[46:49] offset:34816
	v_or_b32_e32 v18, s14, v168
	v_mul_lo_u32 v86, v18, s46
	v_lshl_add_u64 v[18:19], s[18:19], 0, v[86:87]
	v_add_u32_e32 v26, s7, v182
	v_lshl_add_u64 v[18:19], v[18:19], 0, s[24:25]
	v_mul_lo_u32 v86, v26, s46
	v_lshl_add_u64 v[18:19], v[18:19], 0, v[92:93]
	v_lshl_add_u64 v[26:27], s[18:19], 0, v[86:87]
	v_add_u32_e32 v34, s7, v178
	v_lshl_add_u64 v[20:21], v[18:19], 0, s[10:11]
	v_add_co_u32_e32 v18, vcc, s47, v18
	v_lshl_add_u64 v[26:27], v[26:27], 0, s[24:25]
	v_mul_lo_u32 v86, v34, s46
	v_add_u32_e64 v42, s6, 1
	v_addc_co_u32_e32 v19, vcc, 0, v19, vcc
	v_lshl_add_u64 v[26:27], v[26:27], 0, v[92:93]
	v_lshl_add_u64 v[34:35], s[18:19], 0, v[86:87]
	v_lshl_add_u32 v42, v42, 6, v179
	v_lshl_add_u64 v[28:29], v[26:27], 0, s[10:11]
	v_add_co_u32_e32 v26, vcc, s47, v26
	v_lshl_add_u64 v[34:35], v[34:35], 0, s[24:25]
	v_mul_lo_u32 v86, v42, s46
	v_addc_co_u32_e32 v27, vcc, 0, v27, vcc
	v_lshl_add_u64 v[34:35], v[34:35], 0, v[92:93]
	v_lshl_add_u64 v[42:43], s[18:19], 0, v[86:87]
	v_lshl_add_u64 v[36:37], v[34:35], 0, s[10:11]
	v_add_co_u32_e32 v34, vcc, s47, v34
	v_lshl_add_u64 v[42:43], v[42:43], 0, s[24:25]
	s_nop 0
	v_addc_co_u32_e32 v35, vcc, 0, v35, vcc
	v_lshl_add_u64 v[42:43], v[42:43], 0, v[92:93]
	v_lshl_add_u64 v[44:45], v[42:43], 0, s[10:11]
	v_add_co_u32_e32 v42, vcc, s47, v42
	s_waitcnt lgkmcnt(0)
	s_nop 0
	v_addc_co_u32_e32 v43, vcc, 0, v43, vcc
	s_barrier
; #define LAS __attribute__((address_space(3)))
; __device__ __forceinline__ void na_fast_unit(int unit, const bf16_t* P, const float* rpb, bf16_t* AO, LAS unsigned char* lds) {
;     ...
;     for (int s = 0; s < 6; ++s) {
;         LAS unsigned char* buf = lds + (s & 1) * NA_BUF;
;         if (s + 1 < 6) NA_LOAD(s + 1);
;         const bool win = s < 4;
;         f32x4 sc[4];
;         const int kr = rstart + 2 * s + kh;
;         const float* bp = rpb + (h * 15 + (win ? kr - r + 7 : 0)) * 31 - col + 15;
; #pragma unroll
;         for (int j = 0; j < 4; ++j) {
;             if (win && j == 3) { sc[j] = (f32x4){-1.0e30f, -1.0e30f, -1.0e30f, -1.0e30f}; }
;             else { const int lk = 64 * kh + (win ? 16 * (ct0 + j) : 16 * j) + l15;
;                 f32x4 X = (f32x4){0.f, 0.f, 0.f, 0.f};
; #pragma unroll
;                 for (int kk = 0; kk < 4; ++kk) { const bf16x8 kf = *(const LAS bf16x8*)(buf + NA_KB + lk * NA_RSK + (32 * kk + 8 * q) * 2); X = __builtin_amdgcn_mfma_f32_16x16x32_bf16(kf, qf[kk], X, 0, 0, 0); }
;                 if (win) {
; #pragma unroll
;                     for (int rg = 0; rg < 4; ++rg) { const int kc = 16 * (ct0 + j) + 4 * q + rg; const bool ok = kc >= cstart && kc < cstart + 16;
;                         float bias = 0.f; if (ok) bias = bp[kc];
;                         sc[j][rg] = ok ? X[rg] * scale + bias : -1.0e30f; }
	s_sub_i32 s80, s55, s16
	s_mul_i32 s81, s56, 15
	s_add_i32 s80, s80, s52
	s_add_i32 s80, s80, s81
	s_add_i32 s80, s80, 7
	s_mul_i32 s80, s80, 31
	v_or_b32_e32 v244, s33, v169
	v_add_u32_e32 v242, s80, v244
	v_lshlrev_b32_e32 v242, 2, v242
	v_sub_u32_e32 v242, v242, v54
	v_ashrrev_i32_e32 v243, 31, v242
	v_sub_u32_e32 v244, v244, v62
	v_lshl_add_u64 v[240:241], v[242:243], 0, s[64:65]
	v_add_u32_e32 v239, 0, v244
	v_cmp_gt_u32_e32 vcc, 16, v239
	s_and_saveexec_b64 s[86:87], vcc
	global_load_dword v226, v[240:241], off offset:60
	s_or_b64 exec, exec, s[86:87]
	v_add_u32_e32 v239, 1, v244
	v_cmp_gt_u32_e32 vcc, 16, v239
	s_and_saveexec_b64 s[86:87], vcc
	global_load_dword v227, v[240:241], off offset:64
	s_or_b64 exec, exec, s[86:87]
	v_add_u32_e32 v239, 2, v244
	v_cmp_gt_u32_e32 vcc, 16, v239
	s_and_saveexec_b64 s[86:87], vcc
	global_load_dword v229, v[240:241], off offset:68
	s_or_b64 exec, exec, s[86:87]
	v_add_u32_e32 v239, 3, v244
	v_cmp_gt_u32_e32 vcc, 16, v239
	s_and_saveexec_b64 s[86:87], vcc
	global_load_dword v230, v[240:241], off offset:72
	s_or_b64 exec, exec, s[86:87]
	v_add_u32_e32 v239, 16, v244
	v_cmp_gt_u32_e32 vcc, 16, v239
	s_and_saveexec_b64 s[86:87], vcc
	global_load_dword v231, v[240:241], off offset:124
	s_or_b64 exec, exec, s[86:87]
	v_add_u32_e32 v239, 17, v244
	v_cmp_gt_u32_e32 vcc, 16, v239
	s_and_saveexec_b64 s[86:87], vcc
	global_load_dword v232, v[240:241], off offset:128
	s_or_b64 exec, exec, s[86:87]
	v_add_u32_e32 v239, 18, v244
	v_cmp_gt_u32_e32 vcc, 16, v239
	s_and_saveexec_b64 s[86:87], vcc
	global_load_dword v233, v[240:241], off offset:132
	s_or_b64 exec, exec, s[86:87]
	v_add_u32_e32 v239, 19, v244
	v_cmp_gt_u32_e32 vcc, 16, v239
	s_and_saveexec_b64 s[86:87], vcc
	global_load_dword v234, v[240:241], off offset:136
	s_or_b64 exec, exec, s[86:87]
	v_add_u32_e32 v239, 32, v244
	v_cmp_gt_u32_e32 vcc, 16, v239
	s_and_saveexec_b64 s[86:87], vcc
	global_load_dword v235, v[240:241], off offset:188
	s_or_b64 exec, exec, s[86:87]
	v_add_u32_e32 v239, 33, v244
	v_cmp_gt_u32_e32 vcc, 16, v239
	s_and_saveexec_b64 s[86:87], vcc
	global_load_dword v236, v[240:241], off offset:192
	s_or_b64 exec, exec, s[86:87]
	v_add_u32_e32 v239, 34, v244
	v_cmp_gt_u32_e32 vcc, 16, v239
	s_and_saveexec_b64 s[86:87], vcc
	global_load_dword v237, v[240:241], off offset:196
	s_or_b64 exec, exec, s[86:87]
	v_add_u32_e32 v239, 35, v244
	v_cmp_gt_u32_e32 vcc, 16, v239
	s_and_saveexec_b64 s[86:87], vcc
	global_load_dword v238, v[240:241], off offset:200
	s_or_b64 exec, exec, s[86:87]
	global_load_dwordx4 v[22:25], v[18:19], off offset:1024
	s_nop 0
	global_load_dwordx4 v[18:21], v[20:21], off offset:2048
	s_nop 0
	global_load_dwordx4 v[30:33], v[26:27], off offset:1024
	s_nop 0
	global_load_dwordx4 v[26:29], v[28:29], off offset:2048
	s_nop 0
	global_load_dwordx4 v[38:41], v[34:35], off offset:1024
	s_nop 0
	global_load_dwordx4 v[34:37], v[36:37], off offset:2048
	s_nop 0
	global_load_dwordx4 v[46:49], v[42:43], off offset:1024
	s_nop 0
	global_load_dwordx4 v[42:45], v[44:45], off offset:2048
	ds_read_b128 v[50:53], v180
	s_mov_b64 s[20:21], s[64:65]
	v_mov_b32_e32 v55, s21
	v_sub_co_u32_e32 v98, vcc, s20, v54
	ds_read_b128 v[58:61], v180 offset:128
	ds_read_b128 v[66:69], v180 offset:192
	v_subbrev_co_u32_e32 v99, vcc, 0, v55, vcc
	ds_read_b128 v[54:57], v180 offset:64
	s_waitcnt lgkmcnt(3)
	v_mfma_f32_16x16x32_bf16 v[50:53], v[50:53], v[14:17], 0
	v_add_u32_e32 v65, 16, v62
	v_or_b32_e32 v94, s33, v169
	v_cmp_ge_u32_e32 vcc, v94, v62
	s_waitcnt lgkmcnt(0)
	v_mfma_f32_16x16x32_bf16 v[50:53], v[54:57], v[10:13], v[50:53]
	v_cmp_lt_u32_e64 s[6:7], v94, v65
	s_and_b64 s[14:15], vcc, s[6:7]
	s_sub_i32 s6, s55, s16
	v_mfma_f32_16x16x32_bf16 v[50:53], v[58:61], v[6:9], v[50:53]
	s_mul_i32 s17, s56, 15
	s_add_i32 s6, s6, s52
	s_add_i32 s6, s6, s17
	s_add_i32 s6, s6, 7
	s_mul_i32 s42, s6, 31
	v_mfma_f32_16x16x32_bf16 v[50:53], v[66:69], v[2:5], v[50:53]
	s_ashr_i32 s43, s42, 31
	v_mov_b32_e32 v95, v87
	v_lshl_add_u64 v[54:55], s[42:43], 2, v[98:99]
	v_mov_b32_e32 v58, 0xf149f2ca
	v_lshl_add_u64 v[56:57], v[94:95], 2, v[54:55]
	v_mov_b32_e32 v59, 0xf149f2ca
	v_readlane_b32 s61, v254, 30
	v_readlane_b32 s62, v254, 31
	v_readlane_b32 s63, v254, 32
	v_readlane_b32 s66, v254, 35
	v_readlane_b32 s67, v254, 36
	v_readlane_b32 s68, v254, 37
	v_readlane_b32 s69, v254, 38
	v_readlane_b32 s70, v254, 39
	v_readlane_b32 s71, v254, 40
	v_readlane_b32 s72, v254, 41
	v_readlane_b32 s73, v254, 42
	v_readlane_b32 s74, v254, 43
	v_readlane_b32 s75, v254, 44
	s_and_saveexec_b64 s[6:7], s[14:15]
	s_cbranch_execz .LBB0_1216
	s_waitcnt vmcnt(8)
	v_mov_b32_e32 v59, v226
	v_fmac_f32_e32 v59, 0x3db504f3, v50
